# baseline (speedup 1.0000x reference)
.Lskip_late_sleep:
	v_lshrrev_b32_e32 v42, 6, v0
	v_bfe_u32 v41, v0, 5, 1
	v_and_b32_e32 v40, 31, v0
	v_readfirstlane_b32 s23, v42
	v_and_b32_e32 v43, 7, v0
	v_bfe_u32 v44, v0, 3, 3
	s_lshl_b32 s3, s2, 12
	s_lshl_b32 s19, s2, 7
	s_lshl_b32 s23, s23, 12
	v_lshlrev_b32_e32 v1, 11, v41
	v_lshl_or_b32 v1, v40, 2, v1
	s_mov_b32 m0, s23
	v_lshrrev_b32_e32 v46, 1, v44
	v_xor_b32_e32 v46, v43, v46
	v_lshlrev_b32_e32 v46, 4, v46
	v_lshl_add_u32 v35, v44, 16, v46
	v_lshl_add_u32 v35, v42, 21, v35
	v_add_u32_e32 v35, s19, v35
	v_xor_b32_e32 v86, 64, v35
	s_mov_b32 s20, 0x7fc00
	s_mov_b32 s21, 0xff800
	s_mov_b32 s22, 0x17f400
	s_mov_b32 s14, 0x200000
	s_mov_b32 s15, 0x20000
	s_waitcnt lgkmcnt(0)
	s_mov_b32 s12, s6
	s_and_b32 s13, s7, 0xffff
	s_and_b32 s5, s5, 0xffff
	s_mov_b32 s6, 0x800000
	s_mov_b32 s7, s15
	buffer_load_dword v18, v1, s[12:15], s3 offen nt
	buffer_load_dword v19, v1, s[12:15], s3 offen offset:128 nt
	buffer_load_dword v20, v1, s[12:15], s3 offen offset:256 nt
	buffer_load_dword v21, v1, s[12:15], s3 offen offset:384 nt
	buffer_load_dword v22, v1, s[12:15], s3 offen offset:512 nt
	buffer_load_dword v23, v1, s[12:15], s3 offen offset:640 nt
	buffer_load_dword v24, v1, s[12:15], s3 offen offset:768 nt
	buffer_load_dword v25, v1, s[12:15], s3 offen offset:896 nt
	buffer_load_dword v26, v1, s[12:15], s3 offen offset:1024 nt
	buffer_load_dword v27, v1, s[12:15], s3 offen offset:1152 nt
	buffer_load_dword v28, v1, s[12:15], s3 offen offset:1280 nt
	buffer_load_dword v29, v1, s[12:15], s3 offen offset:1408 nt
	buffer_load_dword v30, v1, s[12:15], s3 offen offset:1536 nt
	buffer_load_dword v31, v1, s[12:15], s3 offen offset:1664 nt
	buffer_load_dword v32, v1, s[12:15], s3 offen offset:1792 nt
	buffer_load_dword v33, v1, s[12:15], s3 offen offset:1920 nt
	buffer_load_dwordx4 v35, s[4:7], 0 offen nt lds
	buffer_load_dwordx4 v86, s[4:7], s20 offen offset:1024 nt lds
	buffer_load_dwordx4 v35, s[4:7], s21 offen offset:2048 nt lds
	buffer_load_dwordx4 v86, s[4:7], s22 offen offset:3072 nt lds
	v_and_b32_e32 v45, 63, v0
	v_lshlrev_b32_e32 v36, 2, v40
	v_lshl_add_u32 v36, v41, 18, v36
	v_lshl_add_u32 v36, v42, 21, v36
	v_add_u32_e32 v36, s19, v36
	v_bfe_u32 v47, v40, 1, 3
	v_lshlrev_b32_e32 v39, 2, v41
	v_xor_b32_e32 v39, v39, v47
	v_lshlrev_b32_e32 v39, 4, v39
	v_lshl_add_u32 v39, v40, 7, v39
	v_lshl_add_u32 v39, v42, 12, v39
	v_xor_b32_e32 v81, 16, v39
	v_xor_b32_e32 v82, 32, v39
	v_xor_b32_e32 v83, 48, v39
	v_cmp_gt_u32_e32 vcc, 32, v45
	v_mov_b32_e32 v34, 0xc1600000
	v_mov_b32_e32 v84, 0x3fb8aa3b
	v_mov_b32_e32 v85, 0x3f317218
	v_lshlrev_b32_e32 v36, 4, v43
	v_lshl_add_u32 v36, v44, 16, v36
	v_lshl_add_u32 v36, v42, 21, v36
	v_add_u32_e32 v36, s19, v36
	v_mul_u32_u24_e32 v37, 0x1200, v42
	v_add_u32_e32 v37, 0x4000, v37
	v_mul_u32_u24_e32 v38, 0x90, v40
	v_lshlrev_b32_e32 v87, 4, v41
	v_add3_u32 v38, v37, v38, v87
	v_mul_u32_u24_e32 v87, 0x90, v44
	v_lshlrev_b32_e32 v46, 4, v43
	v_add3_u32 v87, v37, v87, v46
	s_mov_b32 s24, 0x80000
	s_mov_b32 s25, 0x100000
	s_mov_b32 s26, 0x180000
	s_and_b32 s9, s9, 0xffff
	s_mov_b32 s10, s6
	s_mov_b32 s11, s15
	s_waitcnt vmcnt(4)
	v_max3_f32 v48, v18, v19, v20
	v_max3_f32 v50, v21, v22, v23
	v_max3_f32 v48, v48, v24, v25
	v_max3_f32 v50, v50, v26, v27
	v_max3_f32 v48, v48, v28, v29
	v_max3_f32 v50, v50, v30, v31
	v_max3_f32 v48, v48, v32, v33
	v_max_f32_e32 v48, v48, v50
	v_mov_b32_e32 v50, v48
	s_nop 1
	v_permlane32_swap_b32_e32 v48, v50
	v_max_f32_e32 v48, v48, v50
	v_fmamk_f32 v48, v48, 0x3fb8aa3b, v34
	v_pk_fma_f32 v[18:19], v[18:19], v[84:85], v[48:49] op_sel_hi:[1,0,0] neg_lo:[0,0,1] neg_hi:[0,0,1]
	v_exp_f32_e32 v18, v18
	v_exp_f32_e32 v19, v19
	v_pk_fma_f32 v[20:21], v[20:21], v[84:85], v[48:49] op_sel_hi:[1,0,0] neg_lo:[0,0,1] neg_hi:[0,0,1]
	v_exp_f32_e32 v20, v20
	v_exp_f32_e32 v21, v21
	v_pk_fma_f32 v[22:23], v[22:23], v[84:85], v[48:49] op_sel_hi:[1,0,0] neg_lo:[0,0,1] neg_hi:[0,0,1]
	v_exp_f32_e32 v22, v22
	v_exp_f32_e32 v23, v23
	v_pk_fma_f32 v[24:25], v[24:25], v[84:85], v[48:49] op_sel_hi:[1,0,0] neg_lo:[0,0,1] neg_hi:[0,0,1]
	v_exp_f32_e32 v24, v24
	v_exp_f32_e32 v25, v25
	v_pk_fma_f32 v[26:27], v[26:27], v[84:85], v[48:49] op_sel_hi:[1,0,0] neg_lo:[0,0,1] neg_hi:[0,0,1]
	v_exp_f32_e32 v26, v26
	v_exp_f32_e32 v27, v27
	v_pk_fma_f32 v[28:29], v[28:29], v[84:85], v[48:49] op_sel_hi:[1,0,0] neg_lo:[0,0,1] neg_hi:[0,0,1]
	v_exp_f32_e32 v28, v28
	v_exp_f32_e32 v29, v29
	v_pk_fma_f32 v[30:31], v[30:31], v[84:85], v[48:49] op_sel_hi:[1,0,0] neg_lo:[0,0,1] neg_hi:[0,0,1]
	v_exp_f32_e32 v30, v30
	v_exp_f32_e32 v31, v31
	v_pk_fma_f32 v[32:33], v[32:33], v[84:85], v[48:49] op_sel_hi:[1,0,0] neg_lo:[0,0,1] neg_hi:[0,0,1]
	v_exp_f32_e32 v32, v32
	v_exp_f32_e32 v33, v33
	v_pk_add_f32 v[56:57], v[18:19], v[20:21]
	v_pk_add_f32 v[58:59], v[22:23], v[24:25]
	v_pk_add_f32 v[60:61], v[26:27], v[28:29]
	v_pk_add_f32 v[62:63], v[30:31], v[32:33]
	v_pk_add_f32 v[56:57], v[56:57], v[58:59]
	v_pk_add_f32 v[60:61], v[60:61], v[62:63]
	v_pk_add_f32 v[56:57], v[56:57], v[60:61]
	v_add_f32_e32 v50, v56, v57
	v_mov_b32_e32 v51, v50
	s_nop 1
	v_permlane32_swap_b32_e32 v50, v51
	v_add_f32_e32 v50, v50, v51
	v_log_f32_e32 v50, v50
	v_cvt_pk_f16_f32 v40, v18, v19
	v_cvt_pk_f16_f32 v41, v20, v21
	v_cvt_pk_f16_f32 v42, v22, v23
	v_cvt_pk_f16_f32 v43, v24, v25
	v_cvt_pk_f16_f32 v44, v26, v27
	v_cvt_pk_f16_f32 v45, v28, v29
	v_cvt_pk_f16_f32 v46, v30, v31
	v_cvt_pk_f16_f32 v47, v32, v33
	v_add_f32_e32 v50, 0x41600000, v50
	v_mul_f32_e32 v50, 0xbf317218, v50
	v_cndmask_b32_e64 v51, v50, 1.0, vcc
	s_waitcnt vmcnt(0)
	ds_read_b128 v[2:5], v39
	ds_read_b128 v[6:9], v81
	ds_read_b128 v[10:13], v82
	ds_read_b128 v[14:17], v83
	s_waitcnt lgkmcnt(2)
	v_max3_f32 v52, v2, v3, v4
	v_max3_f32 v53, v5, v6, v7
	v_max_f32_e32 v52, v52, v8
	v_max_f32_e32 v53, v53, v9
	s_waitcnt lgkmcnt(0)
	v_max3_f32 v52, v52, v10, v11
	v_max3_f32 v53, v53, v12, v13
	v_max3_f32 v52, v52, v14, v15
	v_max3_f32 v53, v53, v16, v17
	v_max_f32_e32 v52, v52, v53
	v_mov_b32_e32 v53, v52
	s_nop 1
	v_permlane32_swap_b32_e32 v52, v53
	v_max_f32_e32 v52, v52, v53
	v_cndmask_b32_e32 v54, 1.0, v52, vcc
	v_fmamk_f32 v48, v52, 0x3fb8aa3b, v34
	v_pk_fma_f32 v[2:3], v[2:3], v[84:85], v[48:49] op_sel_hi:[1,0,0] neg_lo:[0,0,1] neg_hi:[0,0,1]
	v_mfma_f32_32x32x2_f32 v[64:79], v51, v54, 0
	v_exp_f32_e32 v2, v2
	v_exp_f32_e32 v3, v3
	v_pk_fma_f32 v[4:5], v[4:5], v[84:85], v[48:49] op_sel_hi:[1,0,0] neg_lo:[0,0,1] neg_hi:[0,0,1]
	v_exp_f32_e32 v4, v4
	v_exp_f32_e32 v5, v5
	v_pk_fma_f32 v[6:7], v[6:7], v[84:85], v[48:49] op_sel_hi:[1,0,0] neg_lo:[0,0,1] neg_hi:[0,0,1]
	v_exp_f32_e32 v6, v6
	v_exp_f32_e32 v7, v7
	v_pk_fma_f32 v[8:9], v[8:9], v[84:85], v[48:49] op_sel_hi:[1,0,0] neg_lo:[0,0,1] neg_hi:[0,0,1]
	v_exp_f32_e32 v8, v8
	v_exp_f32_e32 v9, v9
	v_pk_fma_f32 v[10:11], v[10:11], v[84:85], v[48:49] op_sel_hi:[1,0,0] neg_lo:[0,0,1] neg_hi:[0,0,1]
	v_exp_f32_e32 v10, v10
	v_cvt_pk_f16_f32 v56, v2, v3
	v_cvt_pk_f16_f32 v57, v4, v5
	v_cvt_pk_f16_f32 v58, v6, v7
	v_cvt_pk_f16_f32 v59, v8, v9
	v_exp_f32_e32 v11, v11
	v_pk_fma_f32 v[12:13], v[12:13], v[84:85], v[48:49] op_sel_hi:[1,0,0] neg_lo:[0,0,1] neg_hi:[0,0,1]
	v_exp_f32_e32 v12, v12
	v_mfma_f32_32x32x16_f16 v[18:33], v[40:43], v[56:59], 0
	v_exp_f32_e32 v13, v13
	v_pk_fma_f32 v[14:15], v[14:15], v[84:85], v[48:49] op_sel_hi:[1,0,0] neg_lo:[0,0,1] neg_hi:[0,0,1]
	v_exp_f32_e32 v14, v14
	v_exp_f32_e32 v15, v15
	v_pk_fma_f32 v[16:17], v[16:17], v[84:85], v[48:49] op_sel_hi:[1,0,0] neg_lo:[0,0,1] neg_hi:[0,0,1]
	v_exp_f32_e32 v16, v16
	v_exp_f32_e32 v17, v17
	v_cvt_pk_f16_f32 v60, v10, v11
	v_cvt_pk_f16_f32 v61, v12, v13
	v_cvt_pk_f16_f32 v62, v14, v15
	v_cvt_pk_f16_f32 v63, v16, v17
	s_nop 1
	v_mfma_f32_32x32x16_f16 v[18:33], v[44:47], v[60:63], v[18:33]
	s_nop 11
	v_log_f32_e32 v18, v18
	v_log_f32_e32 v19, v19
	v_log_f32_e32 v20, v20
	v_log_f32_e32 v21, v21
	v_log_f32_e32 v22, v22
	v_log_f32_e32 v23, v23
	v_log_f32_e32 v24, v24
	v_log_f32_e32 v25, v25
	v_pk_fma_f32 v[64:65], v[18:19], v[84:85], v[64:65] op_sel:[0,1,0] op_sel_hi:[1,1,1]
	v_log_f32_e32 v26, v26
	v_log_f32_e32 v27, v27
	v_pk_fma_f32 v[66:67], v[20:21], v[84:85], v[66:67] op_sel:[0,1,0] op_sel_hi:[1,1,1]
	ds_write_b128 v38, v[64:67]
	v_log_f32_e32 v28, v28
	v_log_f32_e32 v29, v29
	v_pk_fma_f32 v[68:69], v[22:23], v[84:85], v[68:69] op_sel:[0,1,0] op_sel_hi:[1,1,1]
	v_log_f32_e32 v30, v30
	v_log_f32_e32 v31, v31
	v_pk_fma_f32 v[70:71], v[24:25], v[84:85], v[70:71] op_sel:[0,1,0] op_sel_hi:[1,1,1]
	ds_write_b128 v38, v[68:71] offset:32
	v_log_f32_e32 v32, v32
	v_log_f32_e32 v33, v33
	v_pk_fma_f32 v[72:73], v[26:27], v[84:85], v[72:73] op_sel:[0,1,0] op_sel_hi:[1,1,1]
	v_pk_fma_f32 v[74:75], v[28:29], v[84:85], v[74:75] op_sel:[0,1,0] op_sel_hi:[1,1,1]
	ds_write_b128 v38, v[72:75] offset:64
	v_pk_fma_f32 v[76:77], v[30:31], v[84:85], v[76:77] op_sel:[0,1,0] op_sel_hi:[1,1,1]
	v_pk_fma_f32 v[78:79], v[32:33], v[84:85], v[78:79] op_sel:[0,1,0] op_sel_hi:[1,1,1]
	ds_write_b128 v38, v[76:79] offset:96
	ds_read_b128 v[18:21], v87
	ds_read_b128 v[22:25], v87 offset:1152
	ds_read_b128 v[26:29], v87 offset:2304
	ds_read_b128 v[30:33], v87 offset:3456
	s_waitcnt lgkmcnt(3)
	buffer_store_dwordx4 v[18:21], v36, s[8:11], 0 offen sc1
	s_waitcnt lgkmcnt(2)
	buffer_store_dwordx4 v[22:25], v36, s[8:11], s24 offen sc1
	s_waitcnt lgkmcnt(1)
	buffer_store_dwordx4 v[26:29], v36, s[8:11], s25 offen sc1
	s_waitcnt lgkmcnt(0)
	buffer_store_dwordx4 v[30:33], v36, s[8:11], s26 offen sc1
	s_endpgm

	.amdhsa_kernel _Z16sum_layer_kernelPKfS0_Pf
		.amdhsa_group_segment_fixed_size 34816
		.amdhsa_private_segment_fixed_size 0
		.amdhsa_kernarg_size 24
		.amdhsa_user_sgpr_count 2
		.amdhsa_user_sgpr_dispatch_ptr 0
		.amdhsa_user_sgpr_queue_ptr 0
		.amdhsa_user_sgpr_kernarg_segment_ptr 1
		.amdhsa_user_sgpr_dispatch_id 0
		.amdhsa_user_sgpr_kernarg_preload_length 0
		.amdhsa_user_sgpr_kernarg_preload_offset 0
		.amdhsa_user_sgpr_private_segment_size 0
		.amdhsa_uses_dynamic_stack 0
		.amdhsa_enable_private_segment 0
		.amdhsa_system_sgpr_workgroup_id_x 1
		.amdhsa_system_sgpr_workgroup_id_y 0
		.amdhsa_system_sgpr_workgroup_id_z 0
		.amdhsa_system_sgpr_workgroup_info 0
		.amdhsa_system_vgpr_workitem_id 0
		.amdhsa_next_free_vgpr 88
		.amdhsa_next_free_sgpr 39
		.amdhsa_accum_offset 88
		.amdhsa_reserve_vcc 1
		.amdhsa_float_round_mode_32 0
		.amdhsa_float_round_mode_16_64 0
		.amdhsa_float_denorm_mode_32 3
		.amdhsa_float_denorm_mode_16_64 3
		.amdhsa_dx10_clamp 1
		.amdhsa_ieee_mode 1
		.amdhsa_fp16_overflow 0
		.amdhsa_tg_split 0
		.amdhsa_exception_fp_ieee_invalid_op 0
		.amdhsa_exception_fp_denorm_src 0
		.amdhsa_exception_fp_ieee_div_zero 0
		.amdhsa_exception_fp_ieee_overflow 0
		.amdhsa_exception_fp_ieee_underflow 0
		.amdhsa_exception_fp_ieee_inexact 0
		.amdhsa_exception_int_div_zero 0
	.end_amdhsa_kernel

amdhsa.kernels:
  - .agpr_count:     0
    .args:
      - .address_space:  global
        .offset:         0
        .size:           8
        .value_kind:     global_buffer
      - .address_space:  global
        .offset:         8
        .size:           8
        .value_kind:     global_buffer
      - .address_space:  global
        .offset:         16
        .size:           8
        .value_kind:     global_buffer
    .group_segment_fixed_size: 34816
    .kernarg_segment_align: 8
    .kernarg_segment_size: 24
    .language:       OpenCL C
    .language_version:
      - 2
      - 0
    .max_flat_workgroup_size: 256
    .name:           _Z16sum_layer_kernelPKfS0_Pf
    .private_segment_fixed_size: 0
    .sgpr_count:     45
    .sgpr_spill_count: 0
    .symbol:         _Z16sum_layer_kernelPKfS0_Pf.kd
    .uniform_work_group_size: 1
    .uses_dynamic_stack: false
    .vgpr_count:     88
    .vgpr_spill_count: 0
    .wavefront_size: 64
